# speedup vs baseline: 1.0249x; 1.0033x over previous
.LBB0_65:
	s_or_b64 exec, exec, s[12:13]
	v_mov_b32_e32 v0, 0x20000
	s_waitcnt lgkmcnt(0)
	s_barrier
	ds_read_b96 v[186:188], v0
	v_lshlrev_b32_e32 v0, 10, v193
	s_load_dwordx4 s[12:15], s[0:1], 0x8
	v_and_b32_e32 v0, 0xc00, v0
	v_lshlrev_b32_e32 v1, 1, v193
	s_waitcnt lgkmcnt(0)
	v_readfirstlane_b32 s18, v188
	s_lshl_b32 s2, s18, 5
	v_add_u32_e32 v0, s2, v0
	v_bfe_u32 v109, v193, 4, 2
	v_and_or_b32 v0, v1, 24, v0
	s_lshr_b32 s3, s3, 6
	v_lshlrev_b32_e32 v217, 3, v109
	v_ashrrev_i32_e32 v1, 31, v0
	v_lshl_or_b32 v200, s3, 8, v217
	v_lshlrev_b64 v[4:5], 2, v[0:1]
	v_mov_b32_e32 v201, 0
	v_lshl_add_u64 v[6:7], s[14:15], 0, v[4:5]
	v_lshlrev_b64 v[0:1], 14, v[200:201]
	v_lshl_add_u64 v[0:1], v[6:7], 0, v[0:1]
	global_load_dwordx4 v[8:11], v[0:1], off offset:16
	global_load_dwordx4 v[12:15], v[0:1], off
	v_or_b32_e32 v0, 1, v200
	v_mov_b32_e32 v1, v201
	v_lshlrev_b64 v[0:1], 14, v[0:1]
	v_lshl_add_u64 v[0:1], v[6:7], 0, v[0:1]
	global_load_dwordx4 v[16:19], v[0:1], off offset:16
	global_load_dwordx4 v[20:23], v[0:1], off
	v_or_b32_e32 v0, 2, v200
	v_mov_b32_e32 v1, v201
	v_lshlrev_b64 v[0:1], 14, v[0:1]
	v_lshl_add_u64 v[0:1], v[6:7], 0, v[0:1]
	global_load_dwordx4 v[24:27], v[0:1], off offset:16
	global_load_dwordx4 v[28:31], v[0:1], off
	v_or_b32_e32 v0, 3, v200
	v_mov_b32_e32 v1, v201
	v_lshlrev_b64 v[0:1], 14, v[0:1]
	v_lshl_add_u64 v[0:1], v[6:7], 0, v[0:1]
	global_load_dwordx4 v[32:35], v[0:1], off offset:16
	global_load_dwordx4 v[36:39], v[0:1], off
	v_or_b32_e32 v0, 4, v200
	v_mov_b32_e32 v1, v201
	v_lshlrev_b64 v[0:1], 14, v[0:1]
	v_lshl_add_u64 v[0:1], v[6:7], 0, v[0:1]
	global_load_dwordx4 v[40:43], v[0:1], off offset:16
	global_load_dwordx4 v[44:47], v[0:1], off
	v_or_b32_e32 v0, 5, v200
	v_mov_b32_e32 v1, v201
	v_lshlrev_b64 v[0:1], 14, v[0:1]
	v_lshl_add_u64 v[0:1], v[6:7], 0, v[0:1]
	global_load_dwordx4 v[48:51], v[0:1], off offset:16
	global_load_dwordx4 v[52:55], v[0:1], off
	v_or_b32_e32 v0, 6, v200
	v_mov_b32_e32 v1, v201
	v_lshlrev_b64 v[0:1], 14, v[0:1]
	v_lshl_add_u64 v[0:1], v[6:7], 0, v[0:1]
	global_load_dwordx4 v[56:59], v[0:1], off offset:16
	global_load_dwordx4 v[60:63], v[0:1], off
	v_or_b32_e32 v0, 7, v200
	v_mov_b32_e32 v1, v201
	v_lshlrev_b64 v[0:1], 14, v[0:1]
	v_lshl_add_u64 v[0:1], v[6:7], 0, v[0:1]
	global_load_dwordx4 v[64:67], v[0:1], off offset:16
	global_load_dwordx4 v[68:71], v[0:1], off
	v_mov_b32_e32 v1, v201
	s_lshl_b32 s14, s3, 7
	v_and_b32_e32 v198, 63, v193
	v_lshlrev_b32_e32 v108, 4, v198
	v_lshl_or_b32 v95, s3, 15, v108
	s_lshl_b32 s0, s3, 11
	v_bfe_u32 v207, v193, 3, 3
	s_lshl_b32 s20, s3, 3
	v_or_b32_e32 v208, s20, v207
	v_readfirstlane_b32 s19, v187
	v_and_b32_e32 v150, 7, v193
	s_mov_b32 s15, 0
	v_or_b32_e32 v198, s0, v198
	s_mov_b32 s24, s15
	s_mov_b32 s25, s15
	s_mov_b32 s26, s15
	s_mov_b32 s27, s15
	v_and_b32_e32 v220, 15, v193
	s_lshl_b32 s22, s18, 2
	s_add_i32 s22, s22, s3
	s_lshl_b32 s21, s3, 12
	s_and_b32 s3, s22, 7
	s_ashr_i32 s23, s22, 3
	s_and_b32 s9, s9, 0xffff
	s_add_i32 s23, s23, 16
	v_mov_b32_e32 v202, v201
	v_mov_b32_e32 v203, v201
	s_mov_b32 s11, 0x20000
	s_mov_b32 s10, 0x40000
	s_waitcnt vmcnt(12)
	v_cvt_pk_f16_f32 v231, v12, v20
	v_accvgpr_write_b32 a0, v231
	s_waitcnt vmcnt(8)
	v_cvt_pk_f16_f32 v230, v28, v36
	v_accvgpr_write_b32 a1, v230
	s_waitcnt vmcnt(4)
	v_cvt_pk_f16_f32 v229, v44, v52
	v_accvgpr_write_b32 a2, v229
	s_waitcnt vmcnt(1)
	v_cvt_pk_f16_f32 v0, v56, v64
	v_accvgpr_write_b32 a131, v0
	v_cvt_pk_f16_f32 v0, v40, v48
	v_accvgpr_write_b32 a130, v0
	v_cvt_pk_f16_f32 v0, v24, v32
	v_accvgpr_write_b32 a129, v0
	v_cvt_pk_f16_f32 v0, v8, v16
	v_accvgpr_write_b32 a128, v0
	s_waitcnt vmcnt(0)
	v_cvt_pk_f16_f32 v0, v61, v69
	v_accvgpr_write_b32 a35, v0
	v_cvt_pk_f16_f32 v0, v45, v53
	v_accvgpr_write_b32 a34, v0
	v_cvt_pk_f16_f32 v0, v29, v37
	v_accvgpr_write_b32 a33, v0
	v_cvt_pk_f16_f32 v0, v13, v21
	v_accvgpr_write_b32 a32, v0
	v_cvt_pk_f16_f32 v0, v57, v65
	v_accvgpr_write_b32 a163, v0
	v_cvt_pk_f16_f32 v0, v41, v49
	v_accvgpr_write_b32 a162, v0
	v_cvt_pk_f16_f32 v0, v25, v33
	v_accvgpr_write_b32 a161, v0
	v_cvt_pk_f16_f32 v0, v9, v17
	v_accvgpr_write_b32 a160, v0
	v_cvt_pk_f16_f32 v0, v62, v70
	v_accvgpr_write_b32 a67, v0
	v_cvt_pk_f16_f32 v0, v46, v54
	v_accvgpr_write_b32 a66, v0
	v_cvt_pk_f16_f32 v0, v30, v38
	v_accvgpr_write_b32 a65, v0
	v_cvt_pk_f16_f32 v0, v14, v22
	v_accvgpr_write_b32 a64, v0
	v_cvt_pk_f16_f32 v0, v58, v66
	v_accvgpr_write_b32 a195, v0
	v_cvt_pk_f16_f32 v0, v42, v50
	v_accvgpr_write_b32 a194, v0
	v_cvt_pk_f16_f32 v0, v26, v34
	v_accvgpr_write_b32 a193, v0
	v_cvt_pk_f16_f32 v0, v10, v18
	v_accvgpr_write_b32 a192, v0
	v_cvt_pk_f16_f32 v0, v63, v71
	v_accvgpr_write_b32 a99, v0
	v_cvt_pk_f16_f32 v0, v47, v55
	v_accvgpr_write_b32 a98, v0
	v_cvt_pk_f16_f32 v0, v31, v39
	v_accvgpr_write_b32 a97, v0
	v_cvt_pk_f16_f32 v0, v15, v23
	v_accvgpr_write_b32 a96, v0
	v_cvt_pk_f16_f32 v0, v59, v67
	v_accvgpr_write_b32 a227, v0
	v_cvt_pk_f16_f32 v0, v43, v51
	v_accvgpr_write_b32 a226, v0
	v_cvt_pk_f16_f32 v0, v27, v35
	v_accvgpr_write_b32 a225, v0
	v_cvt_pk_f16_f32 v0, v11, v19
	v_accvgpr_write_b32 a224, v0
	v_or_b32_e32 v0, 32, v200
	v_lshlrev_b64 v[0:1], 14, v[0:1]
	v_lshl_add_u64 v[0:1], v[6:7], 0, v[0:1]
	global_load_dwordx4 v[8:11], v[0:1], off offset:16
	global_load_dwordx4 v[12:15], v[0:1], off
	v_or_b32_e32 v0, 33, v200
	v_mov_b32_e32 v1, v201
	v_lshlrev_b64 v[0:1], 14, v[0:1]
	v_lshl_add_u64 v[0:1], v[6:7], 0, v[0:1]
	global_load_dwordx4 v[16:19], v[0:1], off offset:16
	global_load_dwordx4 v[20:23], v[0:1], off
	v_or_b32_e32 v0, 34, v200
	v_mov_b32_e32 v1, v201
	v_lshlrev_b64 v[0:1], 14, v[0:1]
	v_lshl_add_u64 v[0:1], v[6:7], 0, v[0:1]
	global_load_dwordx4 v[24:27], v[0:1], off offset:16
	global_load_dwordx4 v[28:31], v[0:1], off
	v_or_b32_e32 v0, 35, v200
	v_mov_b32_e32 v1, v201
	v_lshlrev_b64 v[0:1], 14, v[0:1]
	v_lshl_add_u64 v[0:1], v[6:7], 0, v[0:1]
	global_load_dwordx4 v[32:35], v[0:1], off offset:16
	global_load_dwordx4 v[36:39], v[0:1], off
	v_or_b32_e32 v0, 36, v200
	v_mov_b32_e32 v1, v201
	v_lshlrev_b64 v[0:1], 14, v[0:1]
	v_lshl_add_u64 v[0:1], v[6:7], 0, v[0:1]
	global_load_dwordx4 v[40:43], v[0:1], off offset:16
	global_load_dwordx4 v[44:47], v[0:1], off
	v_or_b32_e32 v0, 37, v200
	v_mov_b32_e32 v1, v201
	v_lshlrev_b64 v[0:1], 14, v[0:1]
	v_lshl_add_u64 v[0:1], v[6:7], 0, v[0:1]
	global_load_dwordx4 v[48:51], v[0:1], off offset:16
	global_load_dwordx4 v[52:55], v[0:1], off
	v_or_b32_e32 v0, 38, v200
	v_mov_b32_e32 v1, v201
	v_lshlrev_b64 v[0:1], 14, v[0:1]
	v_lshl_add_u64 v[0:1], v[6:7], 0, v[0:1]
	v_cvt_pk_f16_f32 v228, v60, v68
	global_load_dwordx4 v[56:59], v[0:1], off offset:16
	global_load_dwordx4 v[60:63], v[0:1], off
	v_or_b32_e32 v0, 39, v200
	v_mov_b32_e32 v1, v201
	v_lshlrev_b64 v[0:1], 14, v[0:1]
	v_lshl_add_u64 v[0:1], v[6:7], 0, v[0:1]
	global_load_dwordx4 v[64:67], v[0:1], off offset:16
	global_load_dwordx4 v[68:71], v[0:1], off
	v_mov_b32_e32 v1, v201
	v_accvgpr_write_b32 a3, v228
	s_waitcnt vmcnt(12)
	v_cvt_pk_f16_f32 v206, v12, v20
	v_accvgpr_write_b32 a4, v206
	s_waitcnt vmcnt(8)
	v_cvt_pk_f16_f32 v197, v28, v36
	v_accvgpr_write_b32 a5, v197
	s_waitcnt vmcnt(4)
	v_cvt_pk_f16_f32 v199, v44, v52
	v_accvgpr_write_b32 a6, v199
	s_waitcnt vmcnt(1)
	v_cvt_pk_f16_f32 v0, v56, v64
	v_accvgpr_write_b32 a135, v0
	v_cvt_pk_f16_f32 v0, v40, v48
	v_accvgpr_write_b32 a134, v0
	v_cvt_pk_f16_f32 v0, v24, v32
	v_accvgpr_write_b32 a133, v0
	v_cvt_pk_f16_f32 v0, v8, v16
	v_accvgpr_write_b32 a132, v0
	s_waitcnt vmcnt(0)
	v_cvt_pk_f16_f32 v0, v61, v69
	v_accvgpr_write_b32 a39, v0
	v_cvt_pk_f16_f32 v0, v45, v53
	v_accvgpr_write_b32 a38, v0
	v_cvt_pk_f16_f32 v0, v29, v37
	v_accvgpr_write_b32 a37, v0
	v_cvt_pk_f16_f32 v0, v13, v21
	v_accvgpr_write_b32 a36, v0
	v_cvt_pk_f16_f32 v0, v57, v65
	v_accvgpr_write_b32 a167, v0
	v_cvt_pk_f16_f32 v0, v41, v49
	v_accvgpr_write_b32 a166, v0
	v_cvt_pk_f16_f32 v0, v25, v33
	v_accvgpr_write_b32 a165, v0
	v_cvt_pk_f16_f32 v0, v9, v17
	v_accvgpr_write_b32 a164, v0
	v_cvt_pk_f16_f32 v0, v62, v70
	v_accvgpr_write_b32 a71, v0
	v_cvt_pk_f16_f32 v0, v46, v54
	v_accvgpr_write_b32 a70, v0
	v_cvt_pk_f16_f32 v0, v30, v38
	v_accvgpr_write_b32 a69, v0
	v_cvt_pk_f16_f32 v0, v14, v22
	v_accvgpr_write_b32 a68, v0
	v_cvt_pk_f16_f32 v0, v58, v66
	v_accvgpr_write_b32 a199, v0
	v_cvt_pk_f16_f32 v0, v42, v50
	v_accvgpr_write_b32 a198, v0
	v_cvt_pk_f16_f32 v0, v26, v34
	v_accvgpr_write_b32 a197, v0
	v_cvt_pk_f16_f32 v0, v10, v18
	v_accvgpr_write_b32 a196, v0
	v_cvt_pk_f16_f32 v0, v63, v71
	v_accvgpr_write_b32 a103, v0
	v_cvt_pk_f16_f32 v0, v47, v55
	v_accvgpr_write_b32 a102, v0
	v_cvt_pk_f16_f32 v0, v31, v39
	v_accvgpr_write_b32 a101, v0
	v_cvt_pk_f16_f32 v0, v15, v23
	v_accvgpr_write_b32 a100, v0
	v_cvt_pk_f16_f32 v0, v59, v67
	v_accvgpr_write_b32 a231, v0
	v_cvt_pk_f16_f32 v0, v43, v51
	v_accvgpr_write_b32 a230, v0
	v_cvt_pk_f16_f32 v0, v27, v35
	v_accvgpr_write_b32 a229, v0
	v_cvt_pk_f16_f32 v0, v11, v19
	v_accvgpr_write_b32 a228, v0
	v_or_b32_e32 v0, 64, v200
	v_lshlrev_b64 v[0:1], 14, v[0:1]
	v_lshl_add_u64 v[0:1], v[6:7], 0, v[0:1]
	global_load_dwordx4 v[8:11], v[0:1], off offset:16
	global_load_dwordx4 v[12:15], v[0:1], off
	v_or_b32_e32 v0, 0x41, v200
	v_mov_b32_e32 v1, v201
	v_lshlrev_b64 v[0:1], 14, v[0:1]
	v_lshl_add_u64 v[0:1], v[6:7], 0, v[0:1]
	global_load_dwordx4 v[16:19], v[0:1], off offset:16
	global_load_dwordx4 v[20:23], v[0:1], off
	v_or_b32_e32 v0, 0x42, v200
	v_mov_b32_e32 v1, v201
	v_lshlrev_b64 v[0:1], 14, v[0:1]
	v_lshl_add_u64 v[0:1], v[6:7], 0, v[0:1]
	global_load_dwordx4 v[24:27], v[0:1], off offset:16
	global_load_dwordx4 v[28:31], v[0:1], off
	v_or_b32_e32 v0, 0x43, v200
	v_mov_b32_e32 v1, v201
	v_lshlrev_b64 v[0:1], 14, v[0:1]
	v_lshl_add_u64 v[0:1], v[6:7], 0, v[0:1]
	global_load_dwordx4 v[32:35], v[0:1], off offset:16
	global_load_dwordx4 v[36:39], v[0:1], off
	v_or_b32_e32 v0, 0x44, v200
	v_mov_b32_e32 v1, v201
	v_lshlrev_b64 v[0:1], 14, v[0:1]
	v_lshl_add_u64 v[0:1], v[6:7], 0, v[0:1]
	global_load_dwordx4 v[40:43], v[0:1], off offset:16
	global_load_dwordx4 v[44:47], v[0:1], off
	v_or_b32_e32 v0, 0x45, v200
	v_mov_b32_e32 v1, v201
	v_lshlrev_b64 v[0:1], 14, v[0:1]
	v_lshl_add_u64 v[0:1], v[6:7], 0, v[0:1]
	global_load_dwordx4 v[48:51], v[0:1], off offset:16
	global_load_dwordx4 v[52:55], v[0:1], off
	v_or_b32_e32 v0, 0x46, v200
	v_mov_b32_e32 v1, v201
	v_lshlrev_b64 v[0:1], 14, v[0:1]
	v_lshl_add_u64 v[0:1], v[6:7], 0, v[0:1]
	v_cvt_pk_f16_f32 v205, v60, v68
	global_load_dwordx4 v[56:59], v[0:1], off offset:16
	global_load_dwordx4 v[60:63], v[0:1], off
	v_or_b32_e32 v0, 0x47, v200
	v_mov_b32_e32 v1, v201
	v_lshlrev_b64 v[0:1], 14, v[0:1]
	v_lshl_add_u64 v[0:1], v[6:7], 0, v[0:1]
	global_load_dwordx4 v[64:67], v[0:1], off offset:16
	global_load_dwordx4 v[68:71], v[0:1], off
	v_mov_b32_e32 v1, v201
	v_accvgpr_write_b32 a7, v205
	s_waitcnt vmcnt(12)
	v_cvt_pk_f16_f32 v155, v12, v20
	v_accvgpr_write_b32 a8, v155
	s_waitcnt vmcnt(8)
	v_cvt_pk_f16_f32 v156, v28, v36
	v_accvgpr_write_b32 a9, v156
	s_waitcnt vmcnt(4)
	v_cvt_pk_f16_f32 v157, v44, v52
	v_accvgpr_write_b32 a10, v157
	s_waitcnt vmcnt(1)
	v_cvt_pk_f16_f32 v0, v56, v64
	v_accvgpr_write_b32 a139, v0
	v_cvt_pk_f16_f32 v0, v40, v48
	v_accvgpr_write_b32 a138, v0
	v_cvt_pk_f16_f32 v0, v24, v32
	v_accvgpr_write_b32 a137, v0
	v_cvt_pk_f16_f32 v0, v8, v16
	v_accvgpr_write_b32 a136, v0
	s_waitcnt vmcnt(0)
	v_cvt_pk_f16_f32 v0, v61, v69
	v_accvgpr_write_b32 a43, v0
	v_cvt_pk_f16_f32 v0, v45, v53
	v_accvgpr_write_b32 a42, v0
	v_cvt_pk_f16_f32 v0, v29, v37
	v_accvgpr_write_b32 a41, v0
	v_cvt_pk_f16_f32 v0, v13, v21
	v_accvgpr_write_b32 a40, v0
	v_cvt_pk_f16_f32 v0, v57, v65
	v_accvgpr_write_b32 a171, v0
	v_cvt_pk_f16_f32 v0, v41, v49
	v_accvgpr_write_b32 a170, v0
	v_cvt_pk_f16_f32 v0, v25, v33
	v_accvgpr_write_b32 a169, v0
	v_cvt_pk_f16_f32 v0, v9, v17
	v_accvgpr_write_b32 a168, v0
	v_cvt_pk_f16_f32 v0, v62, v70
	v_accvgpr_write_b32 a75, v0
	v_cvt_pk_f16_f32 v0, v46, v54
	v_accvgpr_write_b32 a74, v0
	v_cvt_pk_f16_f32 v0, v30, v38
	v_accvgpr_write_b32 a73, v0
	v_cvt_pk_f16_f32 v0, v14, v22
	v_accvgpr_write_b32 a72, v0
	v_cvt_pk_f16_f32 v0, v58, v66
	v_accvgpr_write_b32 a203, v0
	v_cvt_pk_f16_f32 v0, v42, v50
	v_accvgpr_write_b32 a202, v0
	v_cvt_pk_f16_f32 v0, v26, v34
	v_accvgpr_write_b32 a201, v0
	v_cvt_pk_f16_f32 v0, v10, v18
	v_accvgpr_write_b32 a200, v0
	v_cvt_pk_f16_f32 v0, v63, v71
	v_accvgpr_write_b32 a107, v0
	v_cvt_pk_f16_f32 v0, v47, v55
	v_accvgpr_write_b32 a106, v0
	v_cvt_pk_f16_f32 v0, v31, v39
	v_accvgpr_write_b32 a105, v0
	v_cvt_pk_f16_f32 v0, v15, v23
	v_accvgpr_write_b32 a104, v0
	v_cvt_pk_f16_f32 v0, v59, v67
	v_accvgpr_write_b32 a235, v0
	v_cvt_pk_f16_f32 v0, v43, v51
	v_accvgpr_write_b32 a234, v0
	v_cvt_pk_f16_f32 v0, v27, v35
	v_accvgpr_write_b32 a233, v0
	v_cvt_pk_f16_f32 v0, v11, v19
	v_accvgpr_write_b32 a232, v0
	v_or_b32_e32 v0, 0x60, v200
	v_lshlrev_b64 v[0:1], 14, v[0:1]
	v_lshl_add_u64 v[0:1], v[6:7], 0, v[0:1]
	global_load_dwordx4 v[8:11], v[0:1], off offset:16
	global_load_dwordx4 v[12:15], v[0:1], off
	v_or_b32_e32 v0, 0x61, v200
	v_mov_b32_e32 v1, v201
	v_lshlrev_b64 v[0:1], 14, v[0:1]
	v_lshl_add_u64 v[0:1], v[6:7], 0, v[0:1]
	global_load_dwordx4 v[16:19], v[0:1], off offset:16
	global_load_dwordx4 v[20:23], v[0:1], off
	v_or_b32_e32 v0, 0x62, v200
	v_mov_b32_e32 v1, v201
	v_lshlrev_b64 v[0:1], 14, v[0:1]
	v_lshl_add_u64 v[0:1], v[6:7], 0, v[0:1]
	global_load_dwordx4 v[24:27], v[0:1], off offset:16
	global_load_dwordx4 v[28:31], v[0:1], off
	v_or_b32_e32 v0, 0x63, v200
	v_mov_b32_e32 v1, v201
	v_lshlrev_b64 v[0:1], 14, v[0:1]
	v_lshl_add_u64 v[0:1], v[6:7], 0, v[0:1]
	global_load_dwordx4 v[32:35], v[0:1], off offset:16
	global_load_dwordx4 v[36:39], v[0:1], off
	v_or_b32_e32 v0, 0x64, v200
	v_mov_b32_e32 v1, v201
	v_lshlrev_b64 v[0:1], 14, v[0:1]
	v_lshl_add_u64 v[0:1], v[6:7], 0, v[0:1]
	global_load_dwordx4 v[40:43], v[0:1], off offset:16
	global_load_dwordx4 v[44:47], v[0:1], off
	v_or_b32_e32 v0, 0x65, v200
	v_mov_b32_e32 v1, v201
	v_lshlrev_b64 v[0:1], 14, v[0:1]
	v_lshl_add_u64 v[0:1], v[6:7], 0, v[0:1]
	global_load_dwordx4 v[48:51], v[0:1], off offset:16
	global_load_dwordx4 v[52:55], v[0:1], off
	v_or_b32_e32 v0, 0x66, v200
	v_mov_b32_e32 v1, v201
	v_lshlrev_b64 v[0:1], 14, v[0:1]
	v_lshl_add_u64 v[0:1], v[6:7], 0, v[0:1]
	v_cvt_pk_f16_f32 v158, v60, v68
	global_load_dwordx4 v[56:59], v[0:1], off offset:16
	global_load_dwordx4 v[60:63], v[0:1], off
	v_or_b32_e32 v0, 0x67, v200
	v_mov_b32_e32 v1, v201
	v_lshlrev_b64 v[0:1], 14, v[0:1]
	v_lshl_add_u64 v[0:1], v[6:7], 0, v[0:1]
	global_load_dwordx4 v[64:67], v[0:1], off offset:16
	global_load_dwordx4 v[68:71], v[0:1], off
	v_mov_b32_e32 v1, v201
	v_accvgpr_write_b32 a11, v158
	s_waitcnt vmcnt(12)
	v_cvt_pk_f16_f32 v122, v12, v20
	v_accvgpr_write_b32 a12, v122
	s_waitcnt vmcnt(8)
	v_cvt_pk_f16_f32 v123, v28, v36
	v_accvgpr_write_b32 a13, v123
	s_waitcnt vmcnt(4)
	v_cvt_pk_f16_f32 v124, v44, v52
	v_accvgpr_write_b32 a14, v124
	s_waitcnt vmcnt(1)
	v_cvt_pk_f16_f32 v0, v56, v64
	v_accvgpr_write_b32 a143, v0
	v_cvt_pk_f16_f32 v0, v40, v48
	v_accvgpr_write_b32 a142, v0
	v_cvt_pk_f16_f32 v0, v24, v32
	v_accvgpr_write_b32 a141, v0
	v_cvt_pk_f16_f32 v0, v8, v16
	v_accvgpr_write_b32 a140, v0
	s_waitcnt vmcnt(0)
	v_cvt_pk_f16_f32 v0, v61, v69
	v_accvgpr_write_b32 a47, v0
	v_cvt_pk_f16_f32 v0, v45, v53
	v_accvgpr_write_b32 a46, v0
	v_cvt_pk_f16_f32 v0, v29, v37
	v_accvgpr_write_b32 a45, v0
	v_cvt_pk_f16_f32 v0, v13, v21
	v_accvgpr_write_b32 a44, v0
	v_cvt_pk_f16_f32 v0, v57, v65
	v_accvgpr_write_b32 a175, v0
	v_cvt_pk_f16_f32 v0, v41, v49
	v_accvgpr_write_b32 a174, v0
	v_cvt_pk_f16_f32 v0, v25, v33
	v_accvgpr_write_b32 a173, v0
	v_cvt_pk_f16_f32 v0, v9, v17
	v_accvgpr_write_b32 a172, v0
	v_cvt_pk_f16_f32 v0, v62, v70
	v_accvgpr_write_b32 a79, v0
	v_cvt_pk_f16_f32 v0, v46, v54
	v_accvgpr_write_b32 a78, v0
	v_cvt_pk_f16_f32 v0, v30, v38
	v_accvgpr_write_b32 a77, v0
	v_cvt_pk_f16_f32 v0, v14, v22
	v_accvgpr_write_b32 a76, v0
	v_cvt_pk_f16_f32 v0, v58, v66
	v_accvgpr_write_b32 a207, v0
	v_cvt_pk_f16_f32 v0, v42, v50
	v_accvgpr_write_b32 a206, v0
	v_cvt_pk_f16_f32 v0, v26, v34
	v_accvgpr_write_b32 a205, v0
	v_cvt_pk_f16_f32 v0, v10, v18
	v_accvgpr_write_b32 a204, v0
	v_cvt_pk_f16_f32 v0, v63, v71
	v_accvgpr_write_b32 a111, v0
	v_cvt_pk_f16_f32 v0, v47, v55
	v_accvgpr_write_b32 a110, v0
	v_cvt_pk_f16_f32 v0, v31, v39
	v_accvgpr_write_b32 a109, v0
	v_cvt_pk_f16_f32 v0, v15, v23
	v_accvgpr_write_b32 a108, v0
	v_cvt_pk_f16_f32 v0, v59, v67
	v_accvgpr_write_b32 a239, v0
	v_cvt_pk_f16_f32 v0, v43, v51
	v_accvgpr_write_b32 a238, v0
	v_cvt_pk_f16_f32 v0, v27, v35
	v_accvgpr_write_b32 a237, v0
	v_cvt_pk_f16_f32 v0, v11, v19
	v_accvgpr_write_b32 a236, v0
	v_or_b32_e32 v0, 0x80, v200
	v_lshlrev_b64 v[0:1], 14, v[0:1]
	v_lshl_add_u64 v[0:1], v[6:7], 0, v[0:1]
	global_load_dwordx4 v[8:11], v[0:1], off offset:16
	global_load_dwordx4 v[12:15], v[0:1], off
	v_or_b32_e32 v0, 0x81, v200
	v_mov_b32_e32 v1, v201
	v_lshlrev_b64 v[0:1], 14, v[0:1]
	v_lshl_add_u64 v[0:1], v[6:7], 0, v[0:1]
	global_load_dwordx4 v[16:19], v[0:1], off offset:16
	global_load_dwordx4 v[20:23], v[0:1], off
	v_or_b32_e32 v0, 0x82, v200
	v_mov_b32_e32 v1, v201
	v_lshlrev_b64 v[0:1], 14, v[0:1]
	v_lshl_add_u64 v[0:1], v[6:7], 0, v[0:1]
	global_load_dwordx4 v[24:27], v[0:1], off offset:16
	global_load_dwordx4 v[28:31], v[0:1], off
	v_or_b32_e32 v0, 0x83, v200
	v_mov_b32_e32 v1, v201
	v_lshlrev_b64 v[0:1], 14, v[0:1]
	v_lshl_add_u64 v[0:1], v[6:7], 0, v[0:1]
	global_load_dwordx4 v[32:35], v[0:1], off offset:16
	global_load_dwordx4 v[36:39], v[0:1], off
	v_or_b32_e32 v0, 0x84, v200
	v_mov_b32_e32 v1, v201
	v_lshlrev_b64 v[0:1], 14, v[0:1]
	v_lshl_add_u64 v[0:1], v[6:7], 0, v[0:1]
	global_load_dwordx4 v[40:43], v[0:1], off offset:16
	global_load_dwordx4 v[44:47], v[0:1], off
	v_or_b32_e32 v0, 0x85, v200
	v_mov_b32_e32 v1, v201
	v_lshlrev_b64 v[0:1], 14, v[0:1]
	v_lshl_add_u64 v[0:1], v[6:7], 0, v[0:1]
	global_load_dwordx4 v[48:51], v[0:1], off offset:16
	global_load_dwordx4 v[52:55], v[0:1], off
	v_or_b32_e32 v0, 0x86, v200
	v_mov_b32_e32 v1, v201
	v_lshlrev_b64 v[0:1], 14, v[0:1]
	v_lshl_add_u64 v[0:1], v[6:7], 0, v[0:1]
	v_cvt_pk_f16_f32 v125, v60, v68
	global_load_dwordx4 v[56:59], v[0:1], off offset:16
	global_load_dwordx4 v[60:63], v[0:1], off
	v_or_b32_e32 v0, 0x87, v200
	v_mov_b32_e32 v1, v201
	v_lshlrev_b64 v[0:1], 14, v[0:1]
	v_lshl_add_u64 v[0:1], v[6:7], 0, v[0:1]
	global_load_dwordx4 v[64:67], v[0:1], off offset:16
	global_load_dwordx4 v[68:71], v[0:1], off
	v_mov_b32_e32 v1, v201
	v_accvgpr_write_b32 a15, v125
	s_waitcnt vmcnt(12)
	v_cvt_pk_f16_f32 v114, v12, v20
	v_cvt_pk_f16_f32 v245, v13, v21
	v_cvt_pk_f16_f32 v235, v14, v22
	v_cvt_pk_f16_f32 v227, v15, v23
	v_accvgpr_write_b32 a16, v114
	v_accvgpr_write_b32 a48, v245
	v_accvgpr_write_b32 a80, v235
	v_accvgpr_write_b32 a112, v227
	s_waitcnt vmcnt(8)
	v_cvt_pk_f16_f32 v115, v28, v36
	v_cvt_pk_f16_f32 v243, v29, v37
	v_cvt_pk_f16_f32 v234, v30, v38
	v_cvt_pk_f16_f32 v226, v31, v39
	v_accvgpr_write_b32 a17, v115
	v_accvgpr_write_b32 a49, v243
	v_accvgpr_write_b32 a81, v234
	v_accvgpr_write_b32 a113, v226
	s_waitcnt vmcnt(4)
	v_cvt_pk_f16_f32 v116, v44, v52
	v_cvt_pk_f16_f32 v241, v45, v53
	v_cvt_pk_f16_f32 v233, v46, v54
	v_cvt_pk_f16_f32 v225, v47, v55
	v_accvgpr_write_b32 a18, v116
	v_accvgpr_write_b32 a50, v241
	v_accvgpr_write_b32 a82, v233
	v_accvgpr_write_b32 a114, v225
	s_waitcnt vmcnt(1)
	v_cvt_pk_f16_f32 v0, v56, v64
	v_accvgpr_write_b32 a147, v0
	v_cvt_pk_f16_f32 v0, v40, v48
	v_accvgpr_write_b32 a146, v0
	v_cvt_pk_f16_f32 v0, v24, v32
	v_accvgpr_write_b32 a145, v0
	v_cvt_pk_f16_f32 v0, v8, v16
	v_accvgpr_write_b32 a144, v0
	v_cvt_pk_f16_f32 v0, v57, v65
	v_accvgpr_write_b32 a179, v0
	v_cvt_pk_f16_f32 v0, v41, v49
	v_accvgpr_write_b32 a178, v0
	v_cvt_pk_f16_f32 v0, v25, v33
	v_accvgpr_write_b32 a177, v0
	v_cvt_pk_f16_f32 v0, v9, v17
	v_accvgpr_write_b32 a176, v0
	v_cvt_pk_f16_f32 v0, v58, v66
	v_accvgpr_write_b32 a211, v0
	v_cvt_pk_f16_f32 v0, v42, v50
	v_accvgpr_write_b32 a210, v0
	v_cvt_pk_f16_f32 v0, v26, v34
	v_accvgpr_write_b32 a209, v0
	v_cvt_pk_f16_f32 v0, v10, v18
	v_accvgpr_write_b32 a208, v0
	s_waitcnt vmcnt(0)
	v_cvt_pk_f16_f32 v0, v63, v71
	v_accvgpr_write_b32 a115, v0
	v_cvt_pk_f16_f32 v0, v59, v67
	v_accvgpr_write_b32 a243, v0
	v_cvt_pk_f16_f32 v0, v43, v51
	v_accvgpr_write_b32 a242, v0
	v_cvt_pk_f16_f32 v0, v27, v35
	v_accvgpr_write_b32 a241, v0
	v_cvt_pk_f16_f32 v0, v11, v19
	v_accvgpr_write_b32 a240, v0
	v_or_b32_e32 v0, 0xa0, v200
	v_lshlrev_b64 v[0:1], 14, v[0:1]
	v_lshl_add_u64 v[0:1], v[6:7], 0, v[0:1]
	global_load_dwordx4 v[8:11], v[0:1], off offset:16
	global_load_dwordx4 v[12:15], v[0:1], off
	v_or_b32_e32 v0, 0xa1, v200
	v_mov_b32_e32 v1, v201
	v_lshlrev_b64 v[0:1], 14, v[0:1]
	v_lshl_add_u64 v[0:1], v[6:7], 0, v[0:1]
	global_load_dwordx4 v[16:19], v[0:1], off offset:16
	global_load_dwordx4 v[20:23], v[0:1], off
	v_or_b32_e32 v0, 0xa2, v200
	v_mov_b32_e32 v1, v201
	v_lshlrev_b64 v[0:1], 14, v[0:1]
	v_lshl_add_u64 v[0:1], v[6:7], 0, v[0:1]
	global_load_dwordx4 v[24:27], v[0:1], off offset:16
	global_load_dwordx4 v[28:31], v[0:1], off
	v_or_b32_e32 v0, 0xa3, v200
	v_mov_b32_e32 v1, v201
	v_lshlrev_b64 v[0:1], 14, v[0:1]
	v_lshl_add_u64 v[0:1], v[6:7], 0, v[0:1]
	global_load_dwordx4 v[32:35], v[0:1], off offset:16
	global_load_dwordx4 v[36:39], v[0:1], off
	v_or_b32_e32 v0, 0xa4, v200
	v_mov_b32_e32 v1, v201
	v_lshlrev_b64 v[0:1], 14, v[0:1]
	v_lshl_add_u64 v[0:1], v[6:7], 0, v[0:1]
	global_load_dwordx4 v[40:43], v[0:1], off offset:16
	global_load_dwordx4 v[44:47], v[0:1], off
	v_or_b32_e32 v0, 0xa5, v200
	v_mov_b32_e32 v1, v201
	v_lshlrev_b64 v[0:1], 14, v[0:1]
	v_lshl_add_u64 v[0:1], v[6:7], 0, v[0:1]
	global_load_dwordx4 v[48:51], v[0:1], off offset:16
	global_load_dwordx4 v[52:55], v[0:1], off
	v_or_b32_e32 v0, 0xa6, v200
	v_mov_b32_e32 v1, v201
	v_lshlrev_b64 v[0:1], 14, v[0:1]
	v_lshl_add_u64 v[0:1], v[6:7], 0, v[0:1]
	v_cvt_pk_f16_f32 v117, v60, v68
	v_cvt_pk_f16_f32 v240, v61, v69
	v_cvt_pk_f16_f32 v232, v62, v70
	global_load_dwordx4 v[56:59], v[0:1], off offset:16
	global_load_dwordx4 v[60:63], v[0:1], off
	v_or_b32_e32 v0, 0xa7, v200
	v_mov_b32_e32 v1, v201
	v_lshlrev_b64 v[0:1], 14, v[0:1]
	v_lshl_add_u64 v[0:1], v[6:7], 0, v[0:1]
	global_load_dwordx4 v[64:67], v[0:1], off offset:16
	global_load_dwordx4 v[68:71], v[0:1], off
	v_or_b32_e32 v0, 0xc0, v200
	v_mov_b32_e32 v1, v201
	v_lshlrev_b64 v[0:1], 14, v[0:1]
	v_lshl_add_u64 v[0:1], v[6:7], 0, v[0:1]
	v_accvgpr_write_b32 a19, v117
	v_accvgpr_write_b32 a51, v240
	v_accvgpr_write_b32 a83, v232
	s_waitcnt vmcnt(13)
	v_cvt_pk_f16_f32 v255, v8, v16
	s_waitcnt vmcnt(12)
	v_cvt_pk_f16_f32 v110, v12, v20
	v_cvt_pk_f16_f32 v204, v13, v21
	v_cvt_pk_f16_f32 v251, v9, v17
	v_cvt_pk_f16_f32 v196, v14, v22
	v_cvt_pk_f16_f32 v247, v10, v18
	v_cvt_pk_f16_f32 v212, v15, v23
	v_cvt_pk_f16_f32 v239, v11, v19
	global_load_dwordx4 v[8:11], v[0:1], off offset:16
	global_load_dwordx4 v[12:15], v[0:1], off
	v_or_b32_e32 v0, 0xc1, v200
	v_mov_b32_e32 v1, v201
	v_lshlrev_b64 v[0:1], 14, v[0:1]
	v_lshl_add_u64 v[0:1], v[6:7], 0, v[0:1]
	global_load_dwordx4 v[16:19], v[0:1], off offset:16
	global_load_dwordx4 v[20:23], v[0:1], off
	v_or_b32_e32 v0, 0xc2, v200
	v_mov_b32_e32 v1, v201
	v_lshlrev_b64 v[0:1], 14, v[0:1]
	v_lshl_add_u64 v[0:1], v[6:7], 0, v[0:1]
	s_waitcnt vmcnt(12)
	v_cvt_pk_f16_f32 v111, v28, v36
	v_cvt_pk_f16_f32 v254, v24, v32
	v_cvt_pk_f16_f32 v180, v29, v37
	v_cvt_pk_f16_f32 v250, v25, v33
	v_cvt_pk_f16_f32 v213, v30, v38
	v_cvt_pk_f16_f32 v246, v26, v34
	v_cvt_pk_f16_f32 v216, v31, v39
	v_cvt_pk_f16_f32 v238, v27, v35
	global_load_dwordx4 v[24:27], v[0:1], off offset:16
	global_load_dwordx4 v[28:31], v[0:1], off
	v_or_b32_e32 v0, 0xc3, v200
	v_mov_b32_e32 v1, v201
	v_lshlrev_b64 v[0:1], 14, v[0:1]
	v_lshl_add_u64 v[0:1], v[6:7], 0, v[0:1]
	global_load_dwordx4 v[32:35], v[0:1], off offset:16
	global_load_dwordx4 v[36:39], v[0:1], off
	v_or_b32_e32 v0, 0xc4, v200
	v_mov_b32_e32 v1, v201
	v_lshlrev_b64 v[0:1], 14, v[0:1]
	v_lshl_add_u64 v[0:1], v[6:7], 0, v[0:1]
	s_waitcnt vmcnt(12)
	v_cvt_pk_f16_f32 v112, v44, v52
	v_cvt_pk_f16_f32 v253, v40, v48
	v_cvt_pk_f16_f32 v181, v45, v53
	v_cvt_pk_f16_f32 v249, v41, v49
	v_cvt_pk_f16_f32 v219, v46, v54
	v_cvt_pk_f16_f32 v244, v42, v50
	v_cvt_pk_f16_f32 v218, v47, v55
	v_cvt_pk_f16_f32 v237, v43, v51
	global_load_dwordx4 v[40:43], v[0:1], off offset:16
	global_load_dwordx4 v[44:47], v[0:1], off
	v_or_b32_e32 v0, 0xc5, v200
	v_mov_b32_e32 v1, v201
	v_lshlrev_b64 v[0:1], 14, v[0:1]
	v_lshl_add_u64 v[0:1], v[6:7], 0, v[0:1]
	global_load_dwordx4 v[48:51], v[0:1], off offset:16
	global_load_dwordx4 v[52:55], v[0:1], off
	v_or_b32_e32 v0, 0xc6, v200
	v_mov_b32_e32 v1, v201
	v_lshlrev_b64 v[0:1], 14, v[0:1]
	v_lshl_add_u64 v[0:1], v[6:7], 0, v[0:1]
	s_waitcnt vmcnt(12)
	v_cvt_pk_f16_f32 v113, v60, v68
	v_cvt_pk_f16_f32 v252, v56, v64
	v_cvt_pk_f16_f32 v183, v61, v69
	v_cvt_pk_f16_f32 v248, v57, v65
	v_cvt_pk_f16_f32 v222, v62, v70
	v_cvt_pk_f16_f32 v242, v58, v66
	v_cvt_pk_f16_f32 v221, v63, v71
	v_cvt_pk_f16_f32 v236, v59, v67
	global_load_dwordx4 v[56:59], v[0:1], off offset:16
	global_load_dwordx4 v[60:63], v[0:1], off
	v_or_b32_e32 v0, 0xc7, v200
	v_mov_b32_e32 v1, v201
	v_lshlrev_b64 v[0:1], 14, v[0:1]
	v_lshl_add_u64 v[0:1], v[6:7], 0, v[0:1]
	global_load_dwordx4 v[64:67], v[0:1], off offset:16
	global_load_dwordx4 v[68:71], v[0:1], off
	v_or_b32_e32 v0, 0xe0, v200
	v_mov_b32_e32 v1, v201
	v_lshlrev_b64 v[0:1], 14, v[0:1]
	v_lshl_add_u64 v[0:1], v[6:7], 0, v[0:1]
	v_accvgpr_write_b32 a20, v110
	v_accvgpr_write_b32 a21, v111
	v_accvgpr_write_b32 a22, v112
	v_accvgpr_write_b32 a23, v113
	v_accvgpr_write_b32 a52, v204
	v_accvgpr_write_b32 a53, v180
	v_accvgpr_write_b32 a54, v181
	v_accvgpr_write_b32 a55, v183
	v_accvgpr_write_b32 a84, v196
	v_accvgpr_write_b32 a85, v213
	v_accvgpr_write_b32 a86, v219
	v_accvgpr_write_b32 a87, v222
	v_accvgpr_write_b32 a116, v212
	v_accvgpr_write_b32 a117, v216
	v_accvgpr_write_b32 a118, v218
	v_accvgpr_write_b32 a119, v221
	v_accvgpr_write_b32 a148, v255
	v_accvgpr_write_b32 a149, v254
	v_accvgpr_write_b32 a150, v253
	v_accvgpr_write_b32 a151, v252
	s_waitcnt vmcnt(13)
	v_cvt_pk_f16_f32 v167, v8, v16
	s_waitcnt vmcnt(12)
	v_cvt_pk_f16_f32 v190, v12, v20
	v_cvt_pk_f16_f32 v146, v13, v21
	v_cvt_pk_f16_f32 v171, v9, v17
	v_cvt_pk_f16_f32 v159, v14, v22
	v_cvt_pk_f16_f32 v176, v10, v18
	v_cvt_pk_f16_f32 v163, v15, v23
	v_cvt_pk_f16_f32 v189, v11, v19
	global_load_dwordx4 v[8:11], v[0:1], off offset:16
	global_load_dwordx4 v[12:15], v[0:1], off
	v_or_b32_e32 v0, 0xe1, v200
	v_mov_b32_e32 v1, v201
	v_lshlrev_b64 v[0:1], 14, v[0:1]
	v_lshl_add_u64 v[0:1], v[6:7], 0, v[0:1]
	global_load_dwordx4 v[16:19], v[0:1], off offset:16
	global_load_dwordx4 v[20:23], v[0:1], off
	v_or_b32_e32 v0, 0xe2, v200
	v_mov_b32_e32 v1, v201
	v_lshlrev_b64 v[0:1], 14, v[0:1]
	v_lshl_add_u64 v[0:1], v[6:7], 0, v[0:1]
	s_waitcnt vmcnt(13)
	v_cvt_pk_f16_f32 v168, v24, v32
	s_waitcnt vmcnt(12)
	v_cvt_pk_f16_f32 v224, v28, v36
	v_cvt_pk_f16_f32 v147, v29, v37
	v_cvt_pk_f16_f32 v172, v25, v33
	v_cvt_pk_f16_f32 v160, v30, v38
	v_cvt_pk_f16_f32 v177, v26, v34
	v_cvt_pk_f16_f32 v164, v31, v39
	v_cvt_pk_f16_f32 v191, v27, v35
	global_load_dwordx4 v[24:27], v[0:1], off offset:16
	global_load_dwordx4 v[28:31], v[0:1], off
	v_or_b32_e32 v0, 0xe3, v200
	v_mov_b32_e32 v1, v201
	v_lshlrev_b64 v[0:1], 14, v[0:1]
	v_lshl_add_u64 v[0:1], v[6:7], 0, v[0:1]
	global_load_dwordx4 v[32:35], v[0:1], off offset:16
	global_load_dwordx4 v[36:39], v[0:1], off
	v_or_b32_e32 v0, 0xe4, v200
	v_mov_b32_e32 v1, v201
	v_lshlrev_b64 v[0:1], 14, v[0:1]
	v_lshl_add_u64 v[0:1], v[6:7], 0, v[0:1]
	s_waitcnt vmcnt(13)
	v_cvt_pk_f16_f32 v169, v40, v48
	s_waitcnt vmcnt(12)
	v_cvt_pk_f16_f32 v223, v44, v52
	v_cvt_pk_f16_f32 v148, v45, v53
	v_cvt_pk_f16_f32 v174, v41, v49
	v_cvt_pk_f16_f32 v161, v46, v54
	v_cvt_pk_f16_f32 v178, v42, v50
	v_cvt_pk_f16_f32 v165, v47, v55
	v_cvt_pk_f16_f32 v192, v43, v51
	global_load_dwordx4 v[40:43], v[0:1], off offset:16
	global_load_dwordx4 v[44:47], v[0:1], off
	v_or_b32_e32 v0, 0xe5, v200
	v_mov_b32_e32 v1, v201
	v_lshlrev_b64 v[0:1], 14, v[0:1]
	v_lshl_add_u64 v[0:1], v[6:7], 0, v[0:1]
	global_load_dwordx4 v[48:51], v[0:1], off offset:16
	global_load_dwordx4 v[52:55], v[0:1], off
	v_or_b32_e32 v0, 0xe6, v200
	v_mov_b32_e32 v1, v201
	v_lshlrev_b64 v[0:1], 14, v[0:1]
	v_lshl_add_u64 v[0:1], v[6:7], 0, v[0:1]
	v_or_b32_e32 v200, 0xe7, v200
	s_waitcnt vmcnt(12)
	v_cvt_pk_f16_f32 v194, v60, v68
	v_cvt_pk_f16_f32 v170, v56, v64
	v_cvt_pk_f16_f32 v149, v61, v69
	v_cvt_pk_f16_f32 v175, v57, v65
	v_cvt_pk_f16_f32 v162, v62, v70
	v_cvt_pk_f16_f32 v179, v58, v66
	v_cvt_pk_f16_f32 v166, v63, v71
	v_cvt_pk_f16_f32 v195, v59, v67
	global_load_dwordx4 v[56:59], v[0:1], off offset:16
	global_load_dwordx4 v[60:63], v[0:1], off
	v_lshlrev_b64 v[0:1], 14, v[200:201]
	v_lshl_add_u64 v[0:1], v[6:7], 0, v[0:1]
	global_load_dwordx4 v[64:67], v[0:1], off offset:16
	global_load_dwordx4 v[68:71], v[0:1], off
	v_or_b32_e32 v200, s14, v217
	v_lshlrev_b64 v[0:1], 14, v[200:201]
	v_accvgpr_write_b32 a24, v190
	v_accvgpr_write_b32 a25, v224
	v_accvgpr_write_b32 a26, v223
	v_accvgpr_write_b32 a27, v194
	v_accvgpr_write_b32 a56, v146
	v_accvgpr_write_b32 a57, v147
	v_accvgpr_write_b32 a58, v148
	v_accvgpr_write_b32 a59, v149
	v_accvgpr_write_b32 a88, v159
	v_accvgpr_write_b32 a89, v160
	v_accvgpr_write_b32 a90, v161
	v_accvgpr_write_b32 a91, v162
	v_accvgpr_write_b32 a120, v163
	v_accvgpr_write_b32 a121, v164
	v_accvgpr_write_b32 a122, v165
	v_accvgpr_write_b32 a123, v166
	v_accvgpr_write_b32 a152, v167
	v_accvgpr_write_b32 a153, v168
	v_accvgpr_write_b32 a154, v169
	v_accvgpr_write_b32 a155, v170
	v_accvgpr_write_b32 a180, v251
	v_accvgpr_write_b32 a181, v250
	v_accvgpr_write_b32 a182, v249
	s_waitcnt vmcnt(13)
	v_cvt_pk_f16_f32 v134, v8, v16
	v_cvt_pk_f16_f32 v138, v9, v17
	v_cvt_pk_f16_f32 v142, v10, v18
	v_cvt_pk_f16_f32 v151, v11, v19
	s_waitcnt vmcnt(12)
	v_cvt_pk_f16_f32 v173, v12, v20
	v_cvt_pk_f16_f32 v118, v13, v21
	v_cvt_pk_f16_f32 v126, v14, v22
	v_cvt_pk_f16_f32 v130, v15, v23
	v_accvgpr_write_b32 a28, v173
	v_accvgpr_write_b32 a60, v118
	v_accvgpr_write_b32 a92, v126
	v_accvgpr_write_b32 a124, v130
	v_accvgpr_write_b32 a156, v134
	v_accvgpr_write_b32 a183, v248
	v_accvgpr_write_b32 a184, v171
	v_accvgpr_write_b32 a185, v172
	v_accvgpr_write_b32 a186, v174
	v_accvgpr_write_b32 a187, v175
	s_waitcnt vmcnt(9)
	v_cvt_pk_f16_f32 v135, v24, v32
	v_cvt_pk_f16_f32 v139, v25, v33
	v_cvt_pk_f16_f32 v143, v26, v34
	v_cvt_pk_f16_f32 v152, v27, v35
	s_waitcnt vmcnt(8)
	v_cvt_pk_f16_f32 v182, v28, v36
	v_cvt_pk_f16_f32 v119, v29, v37
	v_cvt_pk_f16_f32 v127, v30, v38
	v_cvt_pk_f16_f32 v131, v31, v39
	v_accvgpr_write_b32 a29, v182
	v_accvgpr_write_b32 a61, v119
	v_accvgpr_write_b32 a93, v127
	v_accvgpr_write_b32 a125, v131
	v_accvgpr_write_b32 a157, v135
	v_accvgpr_write_b32 a188, v138
	v_accvgpr_write_b32 a189, v139
	v_accvgpr_write_b32 a212, v247
	v_accvgpr_write_b32 a213, v246
	v_accvgpr_write_b32 a214, v244
	s_waitcnt vmcnt(5)
	v_cvt_pk_f16_f32 v136, v40, v48
	v_cvt_pk_f16_f32 v140, v41, v49
	v_cvt_pk_f16_f32 v144, v42, v50
	v_cvt_pk_f16_f32 v153, v43, v51
	s_waitcnt vmcnt(4)
	v_cvt_pk_f16_f32 v184, v44, v52
	v_cvt_pk_f16_f32 v120, v45, v53
	v_cvt_pk_f16_f32 v128, v46, v54
	v_cvt_pk_f16_f32 v132, v47, v55
	v_accvgpr_write_b32 a30, v184
	v_accvgpr_write_b32 a62, v120
	v_accvgpr_write_b32 a94, v128
	v_accvgpr_write_b32 a126, v132
	v_accvgpr_write_b32 a158, v136
	v_accvgpr_write_b32 a190, v140
	v_accvgpr_write_b32 a215, v242
	v_accvgpr_write_b32 a216, v176
	v_accvgpr_write_b32 a217, v177
	s_waitcnt vmcnt(1)
	v_cvt_pk_f16_f32 v137, v56, v64
	v_cvt_pk_f16_f32 v141, v57, v65
	v_lshl_add_u64 v[64:65], s[12:13], 0, v[4:5]
	v_lshl_add_u64 v[0:1], v[64:65], 0, v[0:1]
	global_load_dwordx4 v[4:7], v[0:1], off offset:16
	global_load_dwordx4 v[8:11], v[0:1], off
	v_or_b32_e32 v0, 1, v200
	v_mov_b32_e32 v1, v201
	v_lshlrev_b64 v[0:1], 14, v[0:1]
	v_lshl_add_u64 v[0:1], v[64:65], 0, v[0:1]
	global_load_dwordx4 v[12:15], v[0:1], off offset:16
	global_load_dwordx4 v[16:19], v[0:1], off
	v_or_b32_e32 v0, 2, v200
	v_mov_b32_e32 v1, v201
	v_lshlrev_b64 v[0:1], 14, v[0:1]
	v_lshl_add_u64 v[0:1], v[64:65], 0, v[0:1]
	global_load_dwordx4 v[20:23], v[0:1], off offset:16
	global_load_dwordx4 v[24:27], v[0:1], off
	v_or_b32_e32 v0, 3, v200
	v_mov_b32_e32 v1, v201
	v_lshlrev_b64 v[0:1], 14, v[0:1]
	v_lshl_add_u64 v[0:1], v[64:65], 0, v[0:1]
	global_load_dwordx4 v[28:31], v[0:1], off offset:16
	global_load_dwordx4 v[32:35], v[0:1], off
	v_or_b32_e32 v0, 4, v200
	v_mov_b32_e32 v1, v201
	v_lshlrev_b64 v[0:1], 14, v[0:1]
	v_lshl_add_u64 v[0:1], v[64:65], 0, v[0:1]
	global_load_dwordx4 v[36:39], v[0:1], off offset:16
	global_load_dwordx4 v[40:43], v[0:1], off
	v_or_b32_e32 v0, 5, v200
	v_mov_b32_e32 v1, v201
	v_lshlrev_b64 v[0:1], 14, v[0:1]
	v_lshl_add_u64 v[0:1], v[64:65], 0, v[0:1]
	global_load_dwordx4 v[44:47], v[0:1], off offset:16
	global_load_dwordx4 v[48:51], v[0:1], off
	v_or_b32_e32 v0, 6, v200
	v_mov_b32_e32 v1, v201
	v_lshlrev_b64 v[0:1], 14, v[0:1]
	v_lshl_add_u64 v[0:1], v[64:65], 0, v[0:1]
	v_cvt_pk_f16_f32 v145, v58, v66
	v_cvt_pk_f16_f32 v154, v59, v67
	global_load_dwordx4 v[52:55], v[0:1], off offset:16
	global_load_dwordx4 v[56:59], v[0:1], off
	v_or_b32_e32 v0, 7, v200
	v_mov_b32_e32 v1, v201
	v_lshlrev_b64 v[0:1], 14, v[0:1]
	v_lshl_add_u64 v[0:1], v[64:65], 0, v[0:1]
	s_waitcnt vmcnt(14)
	v_cvt_pk_f16_f32 v209, v60, v68
	v_cvt_pk_f16_f32 v121, v61, v69
	v_cvt_pk_f16_f32 v129, v62, v70
	v_cvt_pk_f16_f32 v133, v63, v71
	global_load_dwordx4 v[60:63], v[0:1], off offset:16
	global_load_dwordx4 v[66:69], v[0:1], off
	v_or_b32_e32 v0, 32, v200
	v_mov_b32_e32 v1, v201
	v_lshlrev_b64 v[0:1], 14, v[0:1]
	v_lshl_add_u64 v[0:1], v[64:65], 0, v[0:1]
	v_readfirstlane_b32 s12, v186
	s_lshl_b32 s13, s19, 3
	v_or_b32_e32 v214, s13, v150
	v_ashrrev_i32_e32 v215, 31, v214
	v_accvgpr_write_b32 a31, v209
	v_accvgpr_write_b32 a63, v121
	v_accvgpr_write_b32 a95, v129
	v_accvgpr_write_b32 a127, v133
	v_accvgpr_write_b32 a159, v137
	v_accvgpr_write_b32 a191, v141
	v_accvgpr_write_b32 a218, v178
	v_accvgpr_write_b32 a219, v179
	v_accvgpr_write_b32 a220, v142
	v_accvgpr_write_b32 a221, v143
	v_accvgpr_write_b32 a222, v144
	v_accvgpr_write_b32 a223, v145
	v_accvgpr_write_b32 a244, v239
	v_accvgpr_write_b32 a245, v238
	v_accvgpr_write_b32 a246, v237
	v_accvgpr_write_b32 a247, v236
	v_accvgpr_write_b32 a248, v189
	v_accvgpr_write_b32 a249, v191
	v_accvgpr_write_b32 a250, v192
	v_accvgpr_write_b32 a251, v195
	v_accvgpr_write_b32 a252, v151
	v_accvgpr_write_b32 a253, v152
	v_accvgpr_write_b32 a254, v153
	v_accvgpr_write_b32 a255, v154
	s_waitcnt vmcnt(13)
	v_cvt_pk_f16_f32 v74, v4, v12
	s_waitcnt vmcnt(12)
	v_cvt_pk_f16_f32 v70, v8, v16
	v_cvt_pk_f16_f32 v78, v9, v17
	v_cvt_pk_f16_f32 v82, v5, v13
	v_cvt_pk_f16_f32 v86, v10, v18
	v_cvt_pk_f16_f32 v2, v6, v14
	v_cvt_pk_f16_f32 v8, v7, v15
	s_waitcnt vmcnt(9)
	v_cvt_pk_f16_f32 v75, v20, v28
	s_waitcnt vmcnt(8)
	v_cvt_pk_f16_f32 v71, v24, v32
	v_cvt_pk_f16_f32 v79, v25, v33
	v_cvt_pk_f16_f32 v83, v21, v29
	v_cvt_pk_f16_f32 v87, v26, v34
	v_cvt_pk_f16_f32 v3, v22, v30
	v_cvt_pk_f16_f32 v27, v27, v35
	v_cvt_pk_f16_f32 v26, v11, v19
	v_cvt_pk_f16_f32 v9, v23, v31
	s_waitcnt vmcnt(5)
	v_cvt_pk_f16_f32 v76, v36, v44
	s_waitcnt vmcnt(4)
	v_cvt_pk_f16_f32 v72, v40, v48
	v_cvt_pk_f16_f32 v80, v41, v49
	v_cvt_pk_f16_f32 v84, v37, v45
	v_cvt_pk_f16_f32 v88, v42, v50
	v_cvt_pk_f16_f32 v4, v38, v46
	v_cvt_pk_f16_f32 v28, v43, v51
	v_cvt_pk_f16_f32 v10, v39, v47
	s_waitcnt vmcnt(1)
	v_cvt_pk_f16_f32 v77, v52, v60
	s_waitcnt vmcnt(0)
	v_cvt_pk_f16_f32 v73, v56, v66
	v_cvt_pk_f16_f32 v81, v57, v67
	v_cvt_pk_f16_f32 v85, v53, v61
	v_cvt_pk_f16_f32 v89, v58, v68
	v_cvt_pk_f16_f32 v5, v54, v62
	v_cvt_pk_f16_f32 v29, v59, v69
	v_cvt_pk_f16_f32 v11, v55, v63
	ds_write_b128 v95, v[70:73]
	ds_write_b128 v95, v[78:81] offset:1024
	ds_write_b128 v95, v[86:89] offset:2048
	ds_write_b128 v95, v[26:29] offset:3072
	ds_write_b128 v95, v[74:77] offset:4096
	ds_write_b128 v95, v[82:85] offset:5120
	ds_write_b128 v95, v[2:5] offset:6144
	ds_write_b128 v95, v[8:11] offset:7168
	global_load_dwordx4 v[4:7], v[0:1], off offset:16
	global_load_dwordx4 v[12:15], v[0:1], off
	v_or_b32_e32 v0, 33, v200
	v_mov_b32_e32 v1, v201
	v_lshlrev_b64 v[0:1], 14, v[0:1]
	v_lshl_add_u64 v[0:1], v[64:65], 0, v[0:1]
	global_load_dwordx4 v[8:11], v[0:1], off offset:16
	global_load_dwordx4 v[16:19], v[0:1], off
	v_or_b32_e32 v0, 34, v200
	v_mov_b32_e32 v1, v201
	v_lshlrev_b64 v[0:1], 14, v[0:1]
	v_lshl_add_u64 v[0:1], v[64:65], 0, v[0:1]
	global_load_dwordx4 v[20:23], v[0:1], off offset:16
	global_load_dwordx4 v[32:35], v[0:1], off
	v_or_b32_e32 v0, 35, v200
	v_mov_b32_e32 v1, v201
	v_lshlrev_b64 v[0:1], 14, v[0:1]
	v_lshl_add_u64 v[0:1], v[64:65], 0, v[0:1]
	global_load_dwordx4 v[24:27], v[0:1], off offset:16
	global_load_dwordx4 v[40:43], v[0:1], off
	v_or_b32_e32 v0, 36, v200
	v_mov_b32_e32 v1, v201
	v_lshlrev_b64 v[0:1], 14, v[0:1]
	v_lshl_add_u64 v[0:1], v[64:65], 0, v[0:1]
	global_load_dwordx4 v[28:31], v[0:1], off offset:16
	global_load_dwordx4 v[44:47], v[0:1], off
	v_or_b32_e32 v0, 37, v200
	v_mov_b32_e32 v1, v201
	v_lshlrev_b64 v[0:1], 14, v[0:1]
	v_lshl_add_u64 v[0:1], v[64:65], 0, v[0:1]
	global_load_dwordx4 v[36:39], v[0:1], off offset:16
	global_load_dwordx4 v[48:51], v[0:1], off
	v_or_b32_e32 v0, 38, v200
	v_mov_b32_e32 v1, v201
	v_lshlrev_b64 v[0:1], 14, v[0:1]
	v_lshl_add_u64 v[0:1], v[64:65], 0, v[0:1]
	global_load_dwordx4 v[52:55], v[0:1], off offset:16
	global_load_dwordx4 v[56:59], v[0:1], off
	v_or_b32_e32 v0, 39, v200
	v_mov_b32_e32 v1, v201
	v_lshlrev_b64 v[0:1], 14, v[0:1]
	v_lshl_add_u64 v[0:1], v[64:65], 0, v[0:1]
	global_load_dwordx4 v[60:63], v[0:1], off offset:16
	global_load_dwordx4 v[66:69], v[0:1], off
	v_or_b32_e32 v0, s0, v193
	v_lshlrev_b32_e32 v94, 4, v0
	v_or_b32_e32 v0, 0x3c00, v94
	v_mov_b32_e32 v1, v201
	v_bfe_u32 v193, v193, 3, 1
	v_cmp_gt_u32_e64 s[0:1], 8, v220
	s_waitcnt vmcnt(13)
	v_cvt_pk_f16_f32 v74, v4, v8
	s_waitcnt vmcnt(12)
	v_cvt_pk_f16_f32 v70, v12, v16
	v_cvt_pk_f16_f32 v78, v13, v17
	v_cvt_pk_f16_f32 v2, v14, v18
	v_cvt_pk_f16_f32 v12, v7, v11
	v_cvt_pk_f16_f32 v82, v5, v9
	v_cvt_pk_f16_f32 v86, v6, v10
	s_waitcnt vmcnt(9)
	v_cvt_pk_f16_f32 v13, v23, v27
	s_waitcnt vmcnt(8)
	v_cvt_pk_f16_f32 v71, v32, v40
	v_cvt_pk_f16_f32 v3, v34, v42
	v_cvt_pk_f16_f32 v34, v15, v19
	v_cvt_pk_f16_f32 v75, v20, v24
	v_cvt_pk_f16_f32 v79, v33, v41
	v_cvt_pk_f16_f32 v83, v21, v25
	v_cvt_pk_f16_f32 v87, v22, v26
	v_cvt_pk_f16_f32 v35, v35, v43
	s_waitcnt vmcnt(5)
	v_cvt_pk_f16_f32 v14, v31, v39
	s_waitcnt vmcnt(4)
	v_cvt_pk_f16_f32 v72, v44, v48
	v_cvt_pk_f16_f32 v76, v28, v36
	v_cvt_pk_f16_f32 v80, v45, v49
	v_cvt_pk_f16_f32 v84, v29, v37
	v_cvt_pk_f16_f32 v4, v46, v50
	v_cvt_pk_f16_f32 v88, v30, v38
	v_cvt_pk_f16_f32 v36, v47, v51
	s_waitcnt vmcnt(1)
	v_cvt_pk_f16_f32 v15, v55, v63
	s_waitcnt vmcnt(0)
	v_cvt_pk_f16_f32 v73, v56, v66
	v_cvt_pk_f16_f32 v77, v52, v60
	v_cvt_pk_f16_f32 v81, v57, v67
	v_cvt_pk_f16_f32 v85, v53, v61
	v_cvt_pk_f16_f32 v5, v58, v68
	v_cvt_pk_f16_f32 v89, v54, v62
	v_cvt_pk_f16_f32 v37, v59, v69
	ds_write_b128 v95, v[70:73] offset:8192
	ds_write_b128 v95, v[78:81] offset:9216
	ds_write_b128 v95, v[2:5] offset:10240
	ds_write_b128 v95, v[34:37] offset:11264
	ds_write_b128 v95, v[74:77] offset:12288
	ds_write_b128 v95, v[82:85] offset:13312
	ds_write_b128 v95, v[86:89] offset:14336
	ds_write_b128 v0, v[12:15]
	v_or_b32_e32 v0, 64, v200
	v_lshlrev_b64 v[0:1], 14, v[0:1]
	v_lshl_add_u64 v[0:1], v[64:65], 0, v[0:1]
	global_load_dwordx4 v[4:7], v[0:1], off offset:16
	global_load_dwordx4 v[8:11], v[0:1], off
	v_or_b32_e32 v0, 0x41, v200
	v_mov_b32_e32 v1, v201
	v_lshlrev_b64 v[0:1], 14, v[0:1]
	v_lshl_add_u64 v[0:1], v[64:65], 0, v[0:1]
	global_load_dwordx4 v[12:15], v[0:1], off offset:16
	global_load_dwordx4 v[16:19], v[0:1], off
	v_or_b32_e32 v0, 0x42, v200
	v_mov_b32_e32 v1, v201
	v_lshlrev_b64 v[0:1], 14, v[0:1]
	v_lshl_add_u64 v[0:1], v[64:65], 0, v[0:1]
	global_load_dwordx4 v[20:23], v[0:1], off offset:16
	global_load_dwordx4 v[28:31], v[0:1], off
	v_or_b32_e32 v0, 0x43, v200
	v_mov_b32_e32 v1, v201
	v_lshlrev_b64 v[0:1], 14, v[0:1]
	v_lshl_add_u64 v[0:1], v[64:65], 0, v[0:1]
	global_load_dwordx4 v[24:27], v[0:1], off offset:16
	global_load_dwordx4 v[32:35], v[0:1], off
	v_or_b32_e32 v0, 0x44, v200
	v_mov_b32_e32 v1, v201
	v_lshlrev_b64 v[0:1], 14, v[0:1]
	v_lshl_add_u64 v[0:1], v[64:65], 0, v[0:1]
	global_load_dwordx4 v[36:39], v[0:1], off offset:16
	global_load_dwordx4 v[40:43], v[0:1], off
	v_or_b32_e32 v0, 0x45, v200
	v_mov_b32_e32 v1, v201
	v_lshlrev_b64 v[0:1], 14, v[0:1]
	v_lshl_add_u64 v[0:1], v[64:65], 0, v[0:1]
	global_load_dwordx4 v[44:47], v[0:1], off offset:16
	global_load_dwordx4 v[48:51], v[0:1], off
	v_or_b32_e32 v0, 0x46, v200
	v_mov_b32_e32 v1, v201
	v_lshlrev_b64 v[0:1], 14, v[0:1]
	v_lshl_add_u64 v[0:1], v[64:65], 0, v[0:1]
	global_load_dwordx4 v[52:55], v[0:1], off offset:16
	global_load_dwordx4 v[56:59], v[0:1], off
	v_or_b32_e32 v0, 0x47, v200
	v_mov_b32_e32 v1, v201
	v_lshlrev_b64 v[0:1], 14, v[0:1]
	v_lshl_add_u64 v[0:1], v[64:65], 0, v[0:1]
	global_load_dwordx4 v[60:63], v[0:1], off offset:16
	global_load_dwordx4 v[66:69], v[0:1], off
	v_or_b32_e32 v0, 0x60, v200
	v_mov_b32_e32 v1, v201
	v_lshlrev_b64 v[0:1], 14, v[0:1]
	v_lshl_add_u64 v[0:1], v[64:65], 0, v[0:1]
	s_waitcnt vmcnt(13)
	v_cvt_pk_f16_f32 v74, v4, v12
	s_waitcnt vmcnt(12)
	v_cvt_pk_f16_f32 v70, v8, v16
	v_cvt_pk_f16_f32 v78, v9, v17
	v_cvt_pk_f16_f32 v82, v5, v13
	v_cvt_pk_f16_f32 v2, v10, v18
	v_cvt_pk_f16_f32 v86, v6, v14
	v_cvt_pk_f16_f32 v8, v7, v15
	s_waitcnt vmcnt(9)
	v_cvt_pk_f16_f32 v75, v20, v24
	s_waitcnt vmcnt(8)
	v_cvt_pk_f16_f32 v71, v28, v32
	v_cvt_pk_f16_f32 v79, v29, v33
	v_cvt_pk_f16_f32 v83, v21, v25
	v_cvt_pk_f16_f32 v3, v30, v34
	v_cvt_pk_f16_f32 v87, v22, v26
	v_cvt_pk_f16_f32 v31, v31, v35
	v_cvt_pk_f16_f32 v30, v11, v19
	v_cvt_pk_f16_f32 v9, v23, v27
	s_waitcnt vmcnt(5)
	v_cvt_pk_f16_f32 v76, v36, v44
	s_waitcnt vmcnt(4)
	v_cvt_pk_f16_f32 v72, v40, v48
	v_cvt_pk_f16_f32 v80, v41, v49
	v_cvt_pk_f16_f32 v84, v37, v45
	v_cvt_pk_f16_f32 v4, v42, v50
	v_cvt_pk_f16_f32 v88, v38, v46
	v_cvt_pk_f16_f32 v32, v43, v51
	v_cvt_pk_f16_f32 v10, v39, v47
	s_waitcnt vmcnt(1)
	v_cvt_pk_f16_f32 v77, v52, v60
	s_waitcnt vmcnt(0)
	v_cvt_pk_f16_f32 v73, v56, v66
	v_cvt_pk_f16_f32 v81, v57, v67
	v_cvt_pk_f16_f32 v85, v53, v61
	v_cvt_pk_f16_f32 v5, v58, v68
	v_cvt_pk_f16_f32 v89, v54, v62
	v_cvt_pk_f16_f32 v33, v59, v69
	v_cvt_pk_f16_f32 v11, v55, v63
	ds_write_b128 v95, v[70:73] offset:16384
	ds_write_b128 v95, v[78:81] offset:17408
	ds_write_b128 v95, v[2:5] offset:18432
	ds_write_b128 v95, v[30:33] offset:19456
	ds_write_b128 v95, v[74:77] offset:20480
	ds_write_b128 v95, v[82:85] offset:21504
	ds_write_b128 v95, v[86:89] offset:22528
	ds_write_b128 v95, v[8:11] offset:23552
	global_load_dwordx4 v[8:11], v[0:1], off offset:16
	global_load_dwordx4 v[40:43], v[0:1], off
	v_or_b32_e32 v0, 0x61, v200
	v_mov_b32_e32 v1, v201
	v_lshlrev_b64 v[0:1], 14, v[0:1]
	v_lshl_add_u64 v[0:1], v[64:65], 0, v[0:1]
	global_load_dwordx4 v[16:19], v[0:1], off offset:16
	global_load_dwordx4 v[48:51], v[0:1], off
	v_or_b32_e32 v0, 0x62, v200
	v_mov_b32_e32 v1, v201
	v_lshlrev_b64 v[0:1], 14, v[0:1]
	v_lshl_add_u64 v[0:1], v[64:65], 0, v[0:1]
	global_load_dwordx4 v[30:33], v[0:1], off offset:16
	global_load_dwordx4 v[56:59], v[0:1], off
	v_or_b32_e32 v0, 0x63, v200
	v_mov_b32_e32 v1, v201
	v_lshlrev_b64 v[0:1], 14, v[0:1]
	v_lshl_add_u64 v[0:1], v[64:65], 0, v[0:1]
	global_load_dwordx4 v[34:37], v[0:1], off offset:16
	global_load_dwordx4 v[60:63], v[0:1], off
	v_or_b32_e32 v0, 0x64, v200
	v_mov_b32_e32 v1, v201
	v_lshlrev_b64 v[0:1], 14, v[0:1]
	v_lshl_add_u64 v[0:1], v[64:65], 0, v[0:1]
	global_load_dwordx4 v[44:47], v[0:1], off offset:16
	global_load_dwordx4 v[72:75], v[0:1], off
	v_or_b32_e32 v0, 0x65, v200
	v_mov_b32_e32 v1, v201
	v_lshlrev_b64 v[0:1], 14, v[0:1]
	v_lshl_add_u64 v[0:1], v[64:65], 0, v[0:1]
	global_load_dwordx4 v[52:55], v[0:1], off offset:16
	global_load_dwordx4 v[80:83], v[0:1], off
	v_or_b32_e32 v0, 0x66, v200
	v_mov_b32_e32 v1, v201
	v_lshlrev_b64 v[0:1], 14, v[0:1]
	v_lshl_add_u64 v[0:1], v[64:65], 0, v[0:1]
	v_or_b32_e32 v200, 0x67, v200
	global_load_dwordx4 v[68:71], v[0:1], off offset:16
	global_load_dwordx4 v[84:87], v[0:1], off
	v_lshlrev_b64 v[0:1], 14, v[200:201]
	v_lshl_add_u64 v[0:1], v[64:65], 0, v[0:1]
	global_load_dwordx4 v[76:79], v[0:1], off offset:16
	s_nop 0
	global_load_dwordx4 v[0:3], v[0:1], off
	v_lshlrev_b32_e32 v200, 5, v109
	s_waitcnt vmcnt(13)
	v_cvt_pk_f16_f32 v4, v8, v16
	s_waitcnt vmcnt(12)
	v_cvt_pk_f16_f32 v64, v40, v48
	v_cvt_pk_f16_f32 v20, v41, v49
	v_cvt_pk_f16_f32 v12, v9, v17
	v_cvt_pk_f16_f32 v28, v42, v50
	v_cvt_pk_f16_f32 v24, v10, v18
	v_cvt_pk_f16_f32 v38, v43, v51
	s_waitcnt vmcnt(9)
	v_cvt_pk_f16_f32 v5, v30, v34
	s_waitcnt vmcnt(8)
	v_cvt_pk_f16_f32 v65, v56, v60
	v_cvt_pk_f16_f32 v13, v31, v35
	v_cvt_pk_f16_f32 v25, v32, v36
	v_cvt_pk_f16_f32 v33, v33, v37
	v_cvt_pk_f16_f32 v32, v11, v19
	v_cvt_pk_f16_f32 v21, v57, v61
	v_cvt_pk_f16_f32 v29, v58, v62
	v_cvt_pk_f16_f32 v39, v59, v63
	s_waitcnt vmcnt(5)
	v_cvt_pk_f16_f32 v26, v46, v54
	v_add_u32_e32 v54, s2, v208
	s_waitcnt vmcnt(4)
	v_cvt_pk_f16_f32 v66, v72, v80
	v_cvt_pk_f16_f32 v34, v47, v55
	v_ashrrev_i32_e32 v55, 31, v54
	v_cvt_pk_f16_f32 v6, v44, v52
	v_cvt_pk_f16_f32 v22, v73, v81
	v_cvt_pk_f16_f32 v14, v45, v53
	v_cvt_pk_f16_f32 v30, v74, v82
	s_waitcnt vmcnt(1)
	v_cvt_pk_f16_f32 v35, v71, v79
	s_waitcnt vmcnt(0)
	v_cvt_pk_f16_f32 v67, v84, v0
	v_or_b32_e32 v0, 0x7c00, v94
	v_cvt_pk_f16_f32 v7, v68, v76
	v_cvt_pk_f16_f32 v23, v85, v1
	v_cvt_pk_f16_f32 v15, v69, v77
	v_cvt_pk_f16_f32 v31, v86, v2
	v_cvt_pk_f16_f32 v27, v70, v78
	v_cvt_pk_f16_f32 v41, v87, v3
	v_cvt_pk_f16_f32 v40, v75, v83
	ds_write_b128 v95, v[64:67] offset:24576
	ds_write_b128 v95, v[20:23] offset:25600
	ds_write_b128 v95, v[28:31] offset:26624
	ds_write_b128 v95, v[38:41] offset:27648
	ds_write_b128 v95, v[4:7] offset:28672
	ds_write_b128 v95, v[12:15] offset:29696
	ds_write_b128 v95, v[24:27] offset:30720
	ds_write_b128 v0, v[32:35]
	v_lshl_add_u64 v[0:1], v[54:55], 2, s[4:5]
	global_load_dword v185, v[0:1], off
	v_add_u32_e32 v0, 0x400, v54
	v_ashrrev_i32_e32 v1, 31, v0
	v_lshl_add_u64 v[0:1], v[0:1], 2, s[4:5]
	global_load_dword v186, v[0:1], off
	v_add_u32_e32 v0, 0x800, v54
	v_ashrrev_i32_e32 v1, 31, v0
	v_lshl_add_u64 v[0:1], v[0:1], 2, s[4:5]
	global_load_dword v187, v[0:1], off
	v_add_u32_e32 v0, 0xc00, v54
	v_ashrrev_i32_e32 v1, 31, v0
	v_lshl_add_u64 v[0:1], v[0:1], 2, s[4:5]
	global_load_dword v188, v[0:1], off
	v_lshlrev_b64 v[0:1], 20, v[214:215]
	v_lshl_add_u64 v[0:1], s[16:17], 0, v[0:1]
	v_lshl_add_u64 v[0:1], s[14:15], 2, v[0:1]
	v_lshl_add_u64 v[210:211], v[0:1], 0, v[200:201]
	global_load_dwordx4 v[4:7], v[210:211], off offset:256
	global_load_dwordx4 v[8:11], v[210:211], off offset:272
	global_load_dwordx4 v[14:17], v[210:211], off offset:384
	global_load_dwordx4 v[18:21], v[210:211], off offset:400
	v_lshlrev_b32_e32 v0, 4, v198
	s_waitcnt lgkmcnt(0)
	s_barrier
	ds_read_b128 v[96:99], v0 offset:23552
	ds_read_b128 v[92:95], v0 offset:22528
	ds_read_b128 v[88:91], v0 offset:21504
	ds_read_b128 v[60:63], v0 offset:20480
	ds_read_b128 v[64:67], v0 offset:19456
	ds_read_b128 v[68:71], v0 offset:18432
	ds_read_b128 v[72:75], v0 offset:17408
	ds_read_b128 v[76:79], v0 offset:16384
	v_mov_b64_e32 v[44:45], s[26:27]
	v_mov_b64_e32 v[40:41], s[26:27]
	v_mov_b64_e32 v[22:23], s[24:25]
	v_mov_b64_e32 v[28:29], s[26:27]
	v_mov_b64_e32 v[32:33], s[26:27]
	v_mov_b64_e32 v[36:37], s[26:27]
	v_mov_b64_e32 v[42:43], s[24:25]
	v_mov_b64_e32 v[38:39], s[24:25]
	v_mov_b64_e32 v[24:25], s[26:27]
	v_mov_b64_e32 v[26:27], s[24:25]
	v_mov_b64_e32 v[30:31], s[24:25]
	v_mov_b64_e32 v[34:35], s[24:25]
	s_or_b32 s4, s3, s13
	s_ashr_i32 s5, s4, 31
	s_lshl_b64 s[4:5], s[4:5], 20
	s_add_u32 s4, s16, s4
	s_addc_u32 s5, s17, s5
	s_cmp_lg_u32 s12, 0
	v_mov_b32_e32 v200, v201
	s_waitcnt vmcnt(3)
	v_cvt_pk_f16_f32 v101, v6, v7
	s_waitcnt vmcnt(2)
	v_cvt_pk_f16_f32 v103, v10, v11
	v_cvt_pk_f16_f32 v102, v8, v9
	v_cvt_pk_f16_f32 v100, v4, v5
	ds_read_b128 v[80:83], v0 offset:31744
	ds_read_b128 v[84:87], v0 offset:30720
	ds_read_b128 v[56:59], v0 offset:29696
	ds_read_b128 v[50:53], v0 offset:28672
	ds_read_b128 v[46:49], v0 offset:27648
	ds_read_b128 v[8:11], v0 offset:26624
	ds_read_b128 v[4:7], v0 offset:25600
	ds_read_b128 v[0:3], v0 offset:24576
	s_waitcnt vmcnt(0)
	v_cvt_pk_f16_f32 v107, v20, v21
	v_cvt_pk_f16_f32 v106, v18, v19
	v_cvt_pk_f16_f32 v105, v16, v17
	v_cvt_pk_f16_f32 v104, v14, v15
	v_mov_b64_e32 v[14:15], s[24:25]
	v_mov_b64_e32 v[18:19], s[24:25]
	v_mov_b64_e32 v[16:17], s[26:27]
	v_mov_b64_e32 v[20:21], s[26:27]
	s_waitcnt lgkmcnt(8)
	s_nop 1
	v_mfma_f32_16x16x32_f16 v[42:45], v[76:79], v[100:103], v[42:45]
	v_mfma_f32_16x16x32_f16 v[38:41], v[72:75], v[100:103], v[38:41]
	v_mfma_f32_16x16x32_f16 v[14:17], v[68:71], v[100:103], v[14:17]
	v_mfma_f32_16x16x32_f16 v[18:21], v[64:67], v[100:103], v[18:21]
	v_mfma_f32_16x16x32_f16 v[22:25], v[60:63], v[100:103], v[22:25]
	v_mfma_f32_16x16x32_f16 v[26:29], v[88:91], v[100:103], v[26:29]
	v_mfma_f32_16x16x32_f16 v[30:33], v[92:95], v[100:103], v[30:33]
	v_mfma_f32_16x16x32_f16 v[34:37], v[96:99], v[100:103], v[34:37]
	v_lshlrev_b32_e32 v103, 4, v150
	s_waitcnt lgkmcnt(0)
	s_nop 1
	v_mfma_f32_16x16x32_f16 v[42:45], v[0:3], v[104:107], v[42:45]
	v_mfma_f32_16x16x32_f16 v[38:41], v[4:7], v[104:107], v[38:41]
	v_mfma_f32_16x16x32_f16 v[14:17], v[8:11], v[104:107], v[14:17]
	v_mfma_f32_16x16x32_f16 v[18:21], v[46:49], v[104:107], v[18:21]
	v_mfma_f32_16x16x32_f16 v[22:25], v[50:53], v[104:107], v[22:25]
	v_mfma_f32_16x16x32_f16 v[26:29], v[56:59], v[104:107], v[26:29]
	v_mfma_f32_16x16x32_f16 v[30:33], v[84:87], v[104:107], v[30:33]
	v_mfma_f32_16x16x32_f16 v[34:37], v[80:83], v[104:107], v[34:37]
	v_lshlrev_b32_e32 v0, 11, v193
	v_mov_b32_e32 v1, v201
	s_nop 15
	s_nop 7
	v_lshl_add_u64 v[0:1], v[210:211], 0, v[0:1]
	v_cndmask_b32_e64 v6, 0, v42, s[0:1]
	v_cndmask_b32_e64 v7, 0, v43, s[0:1]
	v_cndmask_b32_e64 v8, 0, v44, s[0:1]
	v_cndmask_b32_e64 v9, 0, v45, s[0:1]
	v_cndmask_b32_e64 v10, 0, v38, s[0:1]
	v_cndmask_b32_e64 v11, 0, v39, s[0:1]
	v_cndmask_b32_e64 v12, 0, v40, s[0:1]
	v_cndmask_b32_e64 v13, 0, v41, s[0:1]
	global_load_dwordx4 v[50:53], v[0:1], off offset:16
	global_load_dwordx4 v[46:49], v[0:1], off
	global_load_dwordx4 v[42:45], v[0:1], off offset:144
	global_load_dwordx4 v[38:41], v[0:1], off offset:128
	v_lshl_add_u32 v2, v220, 4, s14
	v_lshl_or_b32 v55, v207, 1, v2
	v_or_b32_e32 v2, s13, v220
	v_ashrrev_i32_e32 v3, 31, v2
	v_lshlrev_b32_e32 v0, 7, v109
	v_mov_b32_e32 v109, v201
	v_lshlrev_b64 v[2:3], 21, v[2:3]
	v_or3_b32 v104, v0, v103, s21
	v_lshl_add_u64 v[0:1], s[4:5], 0, v[108:109]
	s_cselect_b64 s[4:5], -1, 0
	v_lshl_add_u64 v[2:3], s[6:7], 0, v[2:3]
	s_ashr_i32 s3, s2, 31
	v_lshl_add_u64 v[2:3], s[2:3], 2, v[2:3]
	v_lshlrev_b32_e32 v4, 2, v208
	v_mov_b32_e32 v5, v201
	v_lshl_add_u64 v[96:97], v[2:3], 0, v[4:5]
	v_lshl_add_u32 v2, v214, 10, v54
	v_ashrrev_i32_e32 v3, 31, v2
	v_lshl_add_u64 v[2:3], v[2:3], 2, s[6:7]
	s_mov_b64 s[2:3], 0x8000000
	v_lshl_add_u64 v[98:99], v[2:3], 0, s[2:3]
	s_mov_b64 s[2:3], 0x8040000
	v_lshl_add_u64 v[100:101], v[2:3], 0, s[2:3]
	s_lshl_b32 s2, s19, 14
	s_lshl_b32 s3, s18, 9
	s_add_i32 s2, s2, s3
	v_mbcnt_lo_u32_b32 v2, -1, 0
	v_add_u32_e32 v106, s2, v55
	v_mbcnt_hi_u32_b32 v2, -1, v2
	v_mov_b64_e32 v[54:55], v[200:201]
	v_mov_b64_e32 v[58:59], v[200:201]
	v_cndmask_b32_e64 v14, 0, v14, s[0:1]
	v_cndmask_b32_e64 v15, 0, v15, s[0:1]
	v_cndmask_b32_e64 v16, 0, v16, s[0:1]
	v_cndmask_b32_e64 v17, 0, v17, s[0:1]
	v_cndmask_b32_e64 v18, 0, v18, s[0:1]
	v_cndmask_b32_e64 v19, 0, v19, s[0:1]
	v_cndmask_b32_e64 v20, 0, v20, s[0:1]
	v_cndmask_b32_e64 v21, 0, v21, s[0:1]
	v_cndmask_b32_e64 v22, 0, v22, s[0:1]
	v_cndmask_b32_e64 v23, 0, v23, s[0:1]
	v_cndmask_b32_e64 v24, 0, v24, s[0:1]
	v_cndmask_b32_e64 v25, 0, v25, s[0:1]
	v_cndmask_b32_e64 v26, 0, v26, s[0:1]
	v_cndmask_b32_e64 v27, 0, v27, s[0:1]
	v_cndmask_b32_e64 v28, 0, v28, s[0:1]
	v_cndmask_b32_e64 v29, 0, v29, s[0:1]
	v_cndmask_b32_e64 v30, 0, v30, s[0:1]
	v_cndmask_b32_e64 v31, 0, v31, s[0:1]
	v_cndmask_b32_e64 v32, 0, v32, s[0:1]
	v_cndmask_b32_e64 v33, 0, v33, s[0:1]
	v_cndmask_b32_e64 v34, 0, v34, s[0:1]
	v_cndmask_b32_e64 v35, 0, v35, s[0:1]
	v_cndmask_b32_e64 v36, 0, v36, s[0:1]
	v_cndmask_b32_e64 v37, 0, v37, s[0:1]
	v_lshlrev_b32_e32 v105, 9, v207
	s_mov_b64 s[6:7], 0
	s_mov_b32 s18, 0x40004000
	v_lshl_or_b32 v107, v2, 2, 32
	v_mov_b32_e32 v108, 0
	v_mov_b64_e32 v[56:57], v[202:203]
	v_mov_b64_e32 v[60:61], v[202:203]
	s_mov_b32 s24, 0
	v_lshl_add_u32 v166, s19, 14, v104
	v_mov_b32_e32 v177, 0
	s_not_b64 s[56:57], s[0:1]
	v_add_u32_e32 v79, 0x200, v166
	s_mov_b32 s37, 0x4038aa3b
	s_mov_b32 s38, 0xbfb8aa3b
	v_lshlrev_b32_e32 v222, 4, v198
	ds_read_b128 v[130:133], v222
	ds_read_b128 v[126:129], v222 offset:1024
	ds_read_b128 v[122:125], v222 offset:2048
	ds_read_b128 v[118:121], v222 offset:3072
	ds_read_b128 v[114:117], v222 offset:4096
	ds_read_b128 v[110:113], v222 offset:5120
	ds_read_b128 v[194:197], v222 offset:6144
	ds_read_b128 v[202:205], v222 offset:7168
	ds_read_b128 v[162:165], v222 offset:8192
	ds_read_b128 v[158:161], v222 offset:9216
	ds_read_b128 v[154:157], v222 offset:10240
	ds_read_b128 v[150:153], v222 offset:11264
	ds_read_b128 v[146:149], v222 offset:12288
	ds_read_b128 v[142:145], v222 offset:13312
	ds_read_b128 v[138:141], v222 offset:14336
	ds_read_b128 v[134:137], v222 offset:15360
	s_waitcnt vmcnt(0)
	v_mul_f32_e32 v185, 0xbfb8aa3b, v185
	v_mul_f32_e32 v186, 0xbfb8aa3b, v186
	v_mul_f32_e32 v187, 0x4038aa3b, v187
	v_mul_f32_e32 v188, 0xbfb8aa3b, v188
	v_cvt_pk_f16_f32 v180, v46, v47
	v_cvt_pk_f16_f32 v181, v48, v49
	v_cvt_pk_f16_f32 v182, v50, v51
	v_cvt_pk_f16_f32 v183, v52, v53
	v_cvt_pk_f16_f32 v218, v38, v39
	v_cvt_pk_f16_f32 v219, v40, v41
	v_cvt_pk_f16_f32 v220, v42, v43
	v_cvt_pk_f16_f32 v221, v44, v45
	s_mov_b32 s25, 1
	v_bitop3_b32 v2, s25, v193, 1 bitop3:0x6c
	v_add_u32_e32 v2, s25, v2
	v_min_i32_e32 v2, 0x1ff, v2
	s_and_b32 s12, s25, 1
	v_lshlrev_b32_e32 v200, 11, v2
	v_lshl_add_u64 v[2:3], v[210:211], 0, v[200:201]
	s_lshl_b32 s14, s12, 8
	v_lshl_add_u64 v[4:5], v[2:3], 0, s[14:15]
	global_load_dwordx4 v[46:49], v[4:5], off
	global_load_dwordx4 v[50:53], v[4:5], off offset:16
	global_load_dwordx4 v[38:41], v[4:5], off offset:128
	global_load_dwordx4 v[42:45], v[4:5], off offset:144
	s_setprio 3
